# non-temporal (streaming) stores for the gate tiles G written by the input-projection epilogue (consumed only several steps later)
# speedup vs baseline: 1.0089x; 1.0069x over previous
.Lpj_sigm:
	v_pk_mul_f32 v[126:127], v[126:127], v[136:137] op_sel_hi:[1,0]
	v_pk_mul_f32 v[128:129], v[128:129], v[136:137] op_sel_hi:[1,0]
	v_pk_mul_f32 v[122:123], v[122:123], v[136:137] op_sel_hi:[1,0]
	v_pk_mul_f32 v[124:125], v[124:125], v[136:137] op_sel_hi:[1,0]
	v_pk_mul_f32 v[144:145], v[126:127], v[186:187]
	v_pk_mul_f32 v[146:147], v[128:129], v[186:187]
	v_pk_mul_f32 v[148:149], v[122:123], v[186:187]
	v_pk_mul_f32 v[150:151], v[124:125], v[186:187]
	v_exp_f32_e32 v144, v144
	v_exp_f32_e32 v145, v145
	v_exp_f32_e32 v146, v146
	v_exp_f32_e32 v147, v147
	v_exp_f32_e32 v148, v148
	v_exp_f32_e32 v149, v149
	v_exp_f32_e32 v150, v150
	v_exp_f32_e32 v151, v151
	s_nop 0
	v_pk_add_f32 v[144:145], v[144:145], v[184:185]
	v_pk_add_f32 v[146:147], v[146:147], v[184:185]
	v_pk_add_f32 v[148:149], v[148:149], v[184:185]
	v_pk_add_f32 v[150:151], v[150:151], v[184:185]
	v_rcp_f32_e32 v144, v144
	v_rcp_f32_e32 v145, v145
	v_rcp_f32_e32 v146, v146
	v_rcp_f32_e32 v147, v147
	v_rcp_f32_e32 v148, v148
	v_rcp_f32_e32 v149, v149
	v_rcp_f32_e32 v150, v150
	v_rcp_f32_e32 v151, v151
	s_nop 0
	v_cvt_pk_bf16_f32 v126, v144, v145
	v_cvt_pk_bf16_f32 v127, v146, v147
	v_cvt_pk_bf16_f32 v128, v148, v149
	v_cvt_pk_bf16_f32 v129, v150, v151
	v_pk_mul_f32 v[118:119], v[118:119], v[136:137] op_sel_hi:[1,0]
	v_pk_mul_f32 v[120:121], v[120:121], v[136:137] op_sel_hi:[1,0]
	v_pk_mul_f32 v[114:115], v[114:115], v[136:137] op_sel_hi:[1,0]
	v_pk_mul_f32 v[116:117], v[116:117], v[136:137] op_sel_hi:[1,0]
	v_pk_mul_f32 v[144:145], v[118:119], v[186:187]
	v_pk_mul_f32 v[146:147], v[120:121], v[186:187]
	v_pk_mul_f32 v[148:149], v[114:115], v[186:187]
	v_pk_mul_f32 v[150:151], v[116:117], v[186:187]
	v_exp_f32_e32 v144, v144
	v_exp_f32_e32 v145, v145
	v_exp_f32_e32 v146, v146
	v_exp_f32_e32 v147, v147
	v_exp_f32_e32 v148, v148
	v_exp_f32_e32 v149, v149
	v_exp_f32_e32 v150, v150
	v_exp_f32_e32 v151, v151
	s_nop 0
	v_pk_add_f32 v[144:145], v[144:145], v[184:185]
	v_pk_add_f32 v[146:147], v[146:147], v[184:185]
	v_pk_add_f32 v[148:149], v[148:149], v[184:185]
	v_pk_add_f32 v[150:151], v[150:151], v[184:185]
	v_rcp_f32_e32 v144, v144
	v_rcp_f32_e32 v145, v145
	v_rcp_f32_e32 v146, v146
	v_rcp_f32_e32 v147, v147
	v_rcp_f32_e32 v148, v148
	v_rcp_f32_e32 v149, v149
	v_rcp_f32_e32 v150, v150
	v_rcp_f32_e32 v151, v151
	s_nop 0
	v_cvt_pk_bf16_f32 v118, v144, v145
	v_cvt_pk_bf16_f32 v119, v146, v147
	v_cvt_pk_bf16_f32 v120, v148, v149
	v_cvt_pk_bf16_f32 v121, v150, v151
	v_mov_b32_e32 v158, v118
	v_mov_b32_e32 v159, v119
	v_mov_b32_e32 v160, v120
	v_mov_b32_e32 v161, v121
	v_mov_b32_dpp v118, v126 row_shl:8 row_mask:0xf bank_mask:0x3
	v_mov_b32_dpp v119, v127 row_shl:8 row_mask:0xf bank_mask:0x3
	v_mov_b32_dpp v120, v128 row_shl:8 row_mask:0xf bank_mask:0x3
	v_mov_b32_dpp v121, v129 row_shl:8 row_mask:0xf bank_mask:0x3
	v_mov_b32_dpp v126, v158 row_shr:8 row_mask:0xf bank_mask:0xc
	v_mov_b32_dpp v127, v159 row_shr:8 row_mask:0xf bank_mask:0xc
	v_mov_b32_dpp v128, v160 row_shr:8 row_mask:0xf bank_mask:0xc
	v_mov_b32_dpp v129, v161 row_shr:8 row_mask:0xf bank_mask:0xc
	s_mul_i32 s28, s22, 0
	v_lshl_add_u64 v[180:181], s[28:29], 0, v[178:179]
	global_store_dwordx4 v[180:181], v[126:129], off nt
	s_mul_i32 s28, s22, 8
	v_lshl_add_u64 v[180:181], s[28:29], 0, v[178:179]
	global_store_dwordx4 v[180:181], v[118:121], off nt
	v_pk_mul_f32 v[110:111], v[110:111], v[136:137] op_sel:[0,1] op_sel_hi:[1,1]
	v_pk_mul_f32 v[112:113], v[112:113], v[136:137] op_sel:[0,1] op_sel_hi:[1,1]
	v_pk_mul_f32 v[106:107], v[106:107], v[136:137] op_sel:[0,1] op_sel_hi:[1,1]
	v_pk_mul_f32 v[108:109], v[108:109], v[136:137] op_sel:[0,1] op_sel_hi:[1,1]
	v_pk_mul_f32 v[144:145], v[110:111], v[186:187]
	v_pk_mul_f32 v[146:147], v[112:113], v[186:187]
	v_pk_mul_f32 v[148:149], v[106:107], v[186:187]
	v_pk_mul_f32 v[150:151], v[108:109], v[186:187]
	v_exp_f32_e32 v144, v144
	v_exp_f32_e32 v145, v145
	v_exp_f32_e32 v146, v146
	v_exp_f32_e32 v147, v147
	v_exp_f32_e32 v148, v148
	v_exp_f32_e32 v149, v149
	v_exp_f32_e32 v150, v150
	v_exp_f32_e32 v151, v151
	s_nop 0
	v_pk_add_f32 v[144:145], v[144:145], v[184:185]
	v_pk_add_f32 v[146:147], v[146:147], v[184:185]
	v_pk_add_f32 v[148:149], v[148:149], v[184:185]
	v_pk_add_f32 v[150:151], v[150:151], v[184:185]
	v_rcp_f32_e32 v144, v144
	v_rcp_f32_e32 v145, v145
	v_rcp_f32_e32 v146, v146
	v_rcp_f32_e32 v147, v147
	v_rcp_f32_e32 v148, v148
	v_rcp_f32_e32 v149, v149
	v_rcp_f32_e32 v150, v150
	v_rcp_f32_e32 v151, v151
	s_nop 0
	v_cvt_pk_bf16_f32 v110, v144, v145
	v_cvt_pk_bf16_f32 v111, v146, v147
	v_cvt_pk_bf16_f32 v112, v148, v149
	v_cvt_pk_bf16_f32 v113, v150, v151
	v_pk_mul_f32 v[102:103], v[102:103], v[136:137] op_sel:[0,1] op_sel_hi:[1,1]
	v_pk_mul_f32 v[104:105], v[104:105], v[136:137] op_sel:[0,1] op_sel_hi:[1,1]
	v_pk_mul_f32 v[98:99], v[98:99], v[136:137] op_sel:[0,1] op_sel_hi:[1,1]
	v_pk_mul_f32 v[100:101], v[100:101], v[136:137] op_sel:[0,1] op_sel_hi:[1,1]
	v_pk_mul_f32 v[144:145], v[102:103], v[186:187]
	v_pk_mul_f32 v[146:147], v[104:105], v[186:187]
	v_pk_mul_f32 v[148:149], v[98:99], v[186:187]
	v_pk_mul_f32 v[150:151], v[100:101], v[186:187]
	v_exp_f32_e32 v144, v144
	v_exp_f32_e32 v145, v145
	v_exp_f32_e32 v146, v146
	v_exp_f32_e32 v147, v147
	v_exp_f32_e32 v148, v148
	v_exp_f32_e32 v149, v149
	v_exp_f32_e32 v150, v150
	v_exp_f32_e32 v151, v151
	s_nop 0
	v_pk_add_f32 v[144:145], v[144:145], v[184:185]
	v_pk_add_f32 v[146:147], v[146:147], v[184:185]
	v_pk_add_f32 v[148:149], v[148:149], v[184:185]
	v_pk_add_f32 v[150:151], v[150:151], v[184:185]
	v_rcp_f32_e32 v144, v144
	v_rcp_f32_e32 v145, v145
	v_rcp_f32_e32 v146, v146
	v_rcp_f32_e32 v147, v147
	v_rcp_f32_e32 v148, v148
	v_rcp_f32_e32 v149, v149
	v_rcp_f32_e32 v150, v150
	v_rcp_f32_e32 v151, v151
	s_nop 0
	v_cvt_pk_bf16_f32 v102, v144, v145
	v_cvt_pk_bf16_f32 v103, v146, v147
	v_cvt_pk_bf16_f32 v104, v148, v149
	v_cvt_pk_bf16_f32 v105, v150, v151
	v_mov_b32_e32 v158, v102
	v_mov_b32_e32 v159, v103
	v_mov_b32_e32 v160, v104
	v_mov_b32_e32 v161, v105
	v_mov_b32_dpp v102, v110 row_shl:8 row_mask:0xf bank_mask:0x3
	v_mov_b32_dpp v103, v111 row_shl:8 row_mask:0xf bank_mask:0x3
	v_mov_b32_dpp v104, v112 row_shl:8 row_mask:0xf bank_mask:0x3
	v_mov_b32_dpp v105, v113 row_shl:8 row_mask:0xf bank_mask:0x3
	v_mov_b32_dpp v110, v158 row_shr:8 row_mask:0xf bank_mask:0xc
	v_mov_b32_dpp v111, v159 row_shr:8 row_mask:0xf bank_mask:0xc
	v_mov_b32_dpp v112, v160 row_shr:8 row_mask:0xf bank_mask:0xc
	v_mov_b32_dpp v113, v161 row_shr:8 row_mask:0xf bank_mask:0xc
	s_mul_i32 s28, s22, 16
	v_lshl_add_u64 v[180:181], s[28:29], 0, v[178:179]
	global_store_dwordx4 v[180:181], v[110:113], off nt
	s_mul_i32 s28, s22, 24
	v_lshl_add_u64 v[180:181], s[28:29], 0, v[178:179]
	global_store_dwordx4 v[180:181], v[102:105], off nt
	v_pk_mul_f32 v[94:95], v[94:95], v[138:139] op_sel_hi:[1,0]
	v_pk_mul_f32 v[96:97], v[96:97], v[138:139] op_sel_hi:[1,0]
	v_pk_mul_f32 v[90:91], v[90:91], v[138:139] op_sel_hi:[1,0]
	v_pk_mul_f32 v[92:93], v[92:93], v[138:139] op_sel_hi:[1,0]
	v_pk_mul_f32 v[144:145], v[94:95], v[186:187]
	v_pk_mul_f32 v[146:147], v[96:97], v[186:187]
	v_pk_mul_f32 v[148:149], v[90:91], v[186:187]
	v_pk_mul_f32 v[150:151], v[92:93], v[186:187]
	v_exp_f32_e32 v144, v144
	v_exp_f32_e32 v145, v145
	v_exp_f32_e32 v146, v146
	v_exp_f32_e32 v147, v147
	v_exp_f32_e32 v148, v148
	v_exp_f32_e32 v149, v149
	v_exp_f32_e32 v150, v150
	v_exp_f32_e32 v151, v151
	s_nop 0
	v_pk_add_f32 v[144:145], v[144:145], v[184:185]
	v_pk_add_f32 v[146:147], v[146:147], v[184:185]
	v_pk_add_f32 v[148:149], v[148:149], v[184:185]
	v_pk_add_f32 v[150:151], v[150:151], v[184:185]
	v_rcp_f32_e32 v144, v144
	v_rcp_f32_e32 v145, v145
	v_rcp_f32_e32 v146, v146
	v_rcp_f32_e32 v147, v147
	v_rcp_f32_e32 v148, v148
	v_rcp_f32_e32 v149, v149
	v_rcp_f32_e32 v150, v150
	v_rcp_f32_e32 v151, v151
	s_nop 0
	v_cvt_pk_bf16_f32 v94, v144, v145
	v_cvt_pk_bf16_f32 v95, v146, v147
	v_cvt_pk_bf16_f32 v96, v148, v149
	v_cvt_pk_bf16_f32 v97, v150, v151
	v_pk_mul_f32 v[86:87], v[86:87], v[138:139] op_sel_hi:[1,0]
	v_pk_mul_f32 v[88:89], v[88:89], v[138:139] op_sel_hi:[1,0]
	v_pk_mul_f32 v[82:83], v[82:83], v[138:139] op_sel_hi:[1,0]
	v_pk_mul_f32 v[84:85], v[84:85], v[138:139] op_sel_hi:[1,0]
	v_pk_mul_f32 v[144:145], v[86:87], v[186:187]
	v_pk_mul_f32 v[146:147], v[88:89], v[186:187]
	v_pk_mul_f32 v[148:149], v[82:83], v[186:187]
	v_pk_mul_f32 v[150:151], v[84:85], v[186:187]
	v_exp_f32_e32 v144, v144
	v_exp_f32_e32 v145, v145
	v_exp_f32_e32 v146, v146
	v_exp_f32_e32 v147, v147
	v_exp_f32_e32 v148, v148
	v_exp_f32_e32 v149, v149
	v_exp_f32_e32 v150, v150
	v_exp_f32_e32 v151, v151
	s_nop 0
	v_pk_add_f32 v[144:145], v[144:145], v[184:185]
	v_pk_add_f32 v[146:147], v[146:147], v[184:185]
	v_pk_add_f32 v[148:149], v[148:149], v[184:185]
	v_pk_add_f32 v[150:151], v[150:151], v[184:185]
	v_rcp_f32_e32 v144, v144
	v_rcp_f32_e32 v145, v145
	v_rcp_f32_e32 v146, v146
	v_rcp_f32_e32 v147, v147
	v_rcp_f32_e32 v148, v148
	v_rcp_f32_e32 v149, v149
	v_rcp_f32_e32 v150, v150
	v_rcp_f32_e32 v151, v151
	s_nop 0
	v_cvt_pk_bf16_f32 v86, v144, v145
	v_cvt_pk_bf16_f32 v87, v146, v147
	v_cvt_pk_bf16_f32 v88, v148, v149
	v_cvt_pk_bf16_f32 v89, v150, v151
	v_mov_b32_e32 v158, v86
	v_mov_b32_e32 v159, v87
	v_mov_b32_e32 v160, v88
	v_mov_b32_e32 v161, v89
	v_mov_b32_dpp v86, v94 row_shl:8 row_mask:0xf bank_mask:0x3
	v_mov_b32_dpp v87, v95 row_shl:8 row_mask:0xf bank_mask:0x3
	v_mov_b32_dpp v88, v96 row_shl:8 row_mask:0xf bank_mask:0x3
	v_mov_b32_dpp v89, v97 row_shl:8 row_mask:0xf bank_mask:0x3
	v_mov_b32_dpp v94, v158 row_shr:8 row_mask:0xf bank_mask:0xc
	v_mov_b32_dpp v95, v159 row_shr:8 row_mask:0xf bank_mask:0xc
	v_mov_b32_dpp v96, v160 row_shr:8 row_mask:0xf bank_mask:0xc
	v_mov_b32_dpp v97, v161 row_shr:8 row_mask:0xf bank_mask:0xc
	s_mul_i32 s28, s22, 32
	v_lshl_add_u64 v[180:181], s[28:29], 0, v[178:179]
	global_store_dwordx4 v[180:181], v[94:97], off nt
	s_mul_i32 s28, s22, 40
	v_lshl_add_u64 v[180:181], s[28:29], 0, v[178:179]
	global_store_dwordx4 v[180:181], v[86:89], off nt
	v_pk_mul_f32 v[78:79], v[78:79], v[138:139] op_sel:[0,1] op_sel_hi:[1,1]
	v_pk_mul_f32 v[80:81], v[80:81], v[138:139] op_sel:[0,1] op_sel_hi:[1,1]
	v_pk_mul_f32 v[74:75], v[74:75], v[138:139] op_sel:[0,1] op_sel_hi:[1,1]
	v_pk_mul_f32 v[76:77], v[76:77], v[138:139] op_sel:[0,1] op_sel_hi:[1,1]
	v_pk_mul_f32 v[144:145], v[78:79], v[186:187]
	v_pk_mul_f32 v[146:147], v[80:81], v[186:187]
	v_pk_mul_f32 v[148:149], v[74:75], v[186:187]
	v_pk_mul_f32 v[150:151], v[76:77], v[186:187]
	v_exp_f32_e32 v144, v144
	v_exp_f32_e32 v145, v145
	v_exp_f32_e32 v146, v146
	v_exp_f32_e32 v147, v147
	v_exp_f32_e32 v148, v148
	v_exp_f32_e32 v149, v149
	v_exp_f32_e32 v150, v150
	v_exp_f32_e32 v151, v151
	s_nop 0
	v_pk_add_f32 v[144:145], v[144:145], v[184:185]
	v_pk_add_f32 v[146:147], v[146:147], v[184:185]
	v_pk_add_f32 v[148:149], v[148:149], v[184:185]
	v_pk_add_f32 v[150:151], v[150:151], v[184:185]
	v_rcp_f32_e32 v144, v144
	v_rcp_f32_e32 v145, v145
	v_rcp_f32_e32 v146, v146
	v_rcp_f32_e32 v147, v147
	v_rcp_f32_e32 v148, v148
	v_rcp_f32_e32 v149, v149
	v_rcp_f32_e32 v150, v150
	v_rcp_f32_e32 v151, v151
	s_nop 0
	v_cvt_pk_bf16_f32 v78, v144, v145
	v_cvt_pk_bf16_f32 v79, v146, v147
	v_cvt_pk_bf16_f32 v80, v148, v149
	v_cvt_pk_bf16_f32 v81, v150, v151
	v_pk_mul_f32 v[70:71], v[70:71], v[138:139] op_sel:[0,1] op_sel_hi:[1,1]
	v_pk_mul_f32 v[72:73], v[72:73], v[138:139] op_sel:[0,1] op_sel_hi:[1,1]
	v_pk_mul_f32 v[66:67], v[66:67], v[138:139] op_sel:[0,1] op_sel_hi:[1,1]
	v_pk_mul_f32 v[68:69], v[68:69], v[138:139] op_sel:[0,1] op_sel_hi:[1,1]
	v_pk_mul_f32 v[144:145], v[70:71], v[186:187]
	v_pk_mul_f32 v[146:147], v[72:73], v[186:187]
	v_pk_mul_f32 v[148:149], v[66:67], v[186:187]
	v_pk_mul_f32 v[150:151], v[68:69], v[186:187]
	v_exp_f32_e32 v144, v144
	v_exp_f32_e32 v145, v145
	v_exp_f32_e32 v146, v146
	v_exp_f32_e32 v147, v147
	v_exp_f32_e32 v148, v148
	v_exp_f32_e32 v149, v149
	v_exp_f32_e32 v150, v150
	v_exp_f32_e32 v151, v151
	s_nop 0
	v_pk_add_f32 v[144:145], v[144:145], v[184:185]
	v_pk_add_f32 v[146:147], v[146:147], v[184:185]
	v_pk_add_f32 v[148:149], v[148:149], v[184:185]
	v_pk_add_f32 v[150:151], v[150:151], v[184:185]
	v_rcp_f32_e32 v144, v144
	v_rcp_f32_e32 v145, v145
	v_rcp_f32_e32 v146, v146
	v_rcp_f32_e32 v147, v147
	v_rcp_f32_e32 v148, v148
	v_rcp_f32_e32 v149, v149
	v_rcp_f32_e32 v150, v150
	v_rcp_f32_e32 v151, v151
	s_nop 0
	v_cvt_pk_bf16_f32 v70, v144, v145
	v_cvt_pk_bf16_f32 v71, v146, v147
	v_cvt_pk_bf16_f32 v72, v148, v149
	v_cvt_pk_bf16_f32 v73, v150, v151
	v_mov_b32_e32 v158, v70
	v_mov_b32_e32 v159, v71
	v_mov_b32_e32 v160, v72
	v_mov_b32_e32 v161, v73
	v_mov_b32_dpp v70, v78 row_shl:8 row_mask:0xf bank_mask:0x3
	v_mov_b32_dpp v71, v79 row_shl:8 row_mask:0xf bank_mask:0x3
	v_mov_b32_dpp v72, v80 row_shl:8 row_mask:0xf bank_mask:0x3
	v_mov_b32_dpp v73, v81 row_shl:8 row_mask:0xf bank_mask:0x3
	v_mov_b32_dpp v78, v158 row_shr:8 row_mask:0xf bank_mask:0xc
	v_mov_b32_dpp v79, v159 row_shr:8 row_mask:0xf bank_mask:0xc
	v_mov_b32_dpp v80, v160 row_shr:8 row_mask:0xf bank_mask:0xc
	v_mov_b32_dpp v81, v161 row_shr:8 row_mask:0xf bank_mask:0xc
	s_mul_i32 s28, s22, 48
	v_lshl_add_u64 v[180:181], s[28:29], 0, v[178:179]
	global_store_dwordx4 v[180:181], v[78:81], off nt
	s_mul_i32 s28, s22, 56
	v_lshl_add_u64 v[180:181], s[28:29], 0, v[178:179]
	global_store_dwordx4 v[180:181], v[70:73], off nt
	v_pk_mul_f32 v[62:63], v[62:63], v[140:141] op_sel_hi:[1,0]
	v_pk_mul_f32 v[64:65], v[64:65], v[140:141] op_sel_hi:[1,0]
	v_pk_mul_f32 v[58:59], v[58:59], v[140:141] op_sel_hi:[1,0]
	v_pk_mul_f32 v[60:61], v[60:61], v[140:141] op_sel_hi:[1,0]
	v_pk_mul_f32 v[144:145], v[62:63], v[186:187]
	v_pk_mul_f32 v[146:147], v[64:65], v[186:187]
	v_pk_mul_f32 v[148:149], v[58:59], v[186:187]
	v_pk_mul_f32 v[150:151], v[60:61], v[186:187]
	v_exp_f32_e32 v144, v144
	v_exp_f32_e32 v145, v145
	v_exp_f32_e32 v146, v146
	v_exp_f32_e32 v147, v147
	v_exp_f32_e32 v148, v148
	v_exp_f32_e32 v149, v149
	v_exp_f32_e32 v150, v150
	v_exp_f32_e32 v151, v151
	s_nop 0
	v_pk_add_f32 v[144:145], v[144:145], v[184:185]
	v_pk_add_f32 v[146:147], v[146:147], v[184:185]
	v_pk_add_f32 v[148:149], v[148:149], v[184:185]
	v_pk_add_f32 v[150:151], v[150:151], v[184:185]
	v_rcp_f32_e32 v144, v144
	v_rcp_f32_e32 v145, v145
	v_rcp_f32_e32 v146, v146
	v_rcp_f32_e32 v147, v147
	v_rcp_f32_e32 v148, v148
	v_rcp_f32_e32 v149, v149
	v_rcp_f32_e32 v150, v150
	v_rcp_f32_e32 v151, v151
	s_nop 0
	v_cvt_pk_bf16_f32 v62, v144, v145
	v_cvt_pk_bf16_f32 v63, v146, v147
	v_cvt_pk_bf16_f32 v64, v148, v149
	v_cvt_pk_bf16_f32 v65, v150, v151
	v_pk_mul_f32 v[54:55], v[54:55], v[140:141] op_sel_hi:[1,0]
	v_pk_mul_f32 v[56:57], v[56:57], v[140:141] op_sel_hi:[1,0]
	v_pk_mul_f32 v[50:51], v[50:51], v[140:141] op_sel_hi:[1,0]
	v_pk_mul_f32 v[52:53], v[52:53], v[140:141] op_sel_hi:[1,0]
	v_pk_mul_f32 v[144:145], v[54:55], v[186:187]
	v_pk_mul_f32 v[146:147], v[56:57], v[186:187]
	v_pk_mul_f32 v[148:149], v[50:51], v[186:187]
	v_pk_mul_f32 v[150:151], v[52:53], v[186:187]
	v_exp_f32_e32 v144, v144
	v_exp_f32_e32 v145, v145
	v_exp_f32_e32 v146, v146
	v_exp_f32_e32 v147, v147
	v_exp_f32_e32 v148, v148
	v_exp_f32_e32 v149, v149
	v_exp_f32_e32 v150, v150
	v_exp_f32_e32 v151, v151
	s_nop 0
	v_pk_add_f32 v[144:145], v[144:145], v[184:185]
	v_pk_add_f32 v[146:147], v[146:147], v[184:185]
	v_pk_add_f32 v[148:149], v[148:149], v[184:185]
	v_pk_add_f32 v[150:151], v[150:151], v[184:185]
	v_rcp_f32_e32 v144, v144
	v_rcp_f32_e32 v145, v145
	v_rcp_f32_e32 v146, v146
	v_rcp_f32_e32 v147, v147
	v_rcp_f32_e32 v148, v148
	v_rcp_f32_e32 v149, v149
	v_rcp_f32_e32 v150, v150
	v_rcp_f32_e32 v151, v151
	s_nop 0
	v_cvt_pk_bf16_f32 v54, v144, v145
	v_cvt_pk_bf16_f32 v55, v146, v147
	v_cvt_pk_bf16_f32 v56, v148, v149
	v_cvt_pk_bf16_f32 v57, v150, v151
	v_mov_b32_e32 v158, v54
	v_mov_b32_e32 v159, v55
	v_mov_b32_e32 v160, v56
	v_mov_b32_e32 v161, v57
	v_mov_b32_dpp v54, v62 row_shl:8 row_mask:0xf bank_mask:0x3
	v_mov_b32_dpp v55, v63 row_shl:8 row_mask:0xf bank_mask:0x3
	v_mov_b32_dpp v56, v64 row_shl:8 row_mask:0xf bank_mask:0x3
	v_mov_b32_dpp v57, v65 row_shl:8 row_mask:0xf bank_mask:0x3
	v_mov_b32_dpp v62, v158 row_shr:8 row_mask:0xf bank_mask:0xc
	v_mov_b32_dpp v63, v159 row_shr:8 row_mask:0xf bank_mask:0xc
	v_mov_b32_dpp v64, v160 row_shr:8 row_mask:0xf bank_mask:0xc
	v_mov_b32_dpp v65, v161 row_shr:8 row_mask:0xf bank_mask:0xc
	s_mul_i32 s28, s22, 128
	v_lshl_add_u64 v[180:181], s[28:29], 0, v[178:179]
	global_store_dwordx4 v[180:181], v[62:65], off nt
	s_mul_i32 s28, s22, 136
	v_lshl_add_u64 v[180:181], s[28:29], 0, v[178:179]
	global_store_dwordx4 v[180:181], v[54:57], off nt
	v_pk_mul_f32 v[46:47], v[46:47], v[140:141] op_sel:[0,1] op_sel_hi:[1,1]
	v_pk_mul_f32 v[48:49], v[48:49], v[140:141] op_sel:[0,1] op_sel_hi:[1,1]
	v_pk_mul_f32 v[42:43], v[42:43], v[140:141] op_sel:[0,1] op_sel_hi:[1,1]
	v_pk_mul_f32 v[44:45], v[44:45], v[140:141] op_sel:[0,1] op_sel_hi:[1,1]
	v_pk_mul_f32 v[144:145], v[46:47], v[186:187]
	v_pk_mul_f32 v[146:147], v[48:49], v[186:187]
	v_pk_mul_f32 v[148:149], v[42:43], v[186:187]
	v_pk_mul_f32 v[150:151], v[44:45], v[186:187]
	v_exp_f32_e32 v144, v144
	v_exp_f32_e32 v145, v145
	v_exp_f32_e32 v146, v146
	v_exp_f32_e32 v147, v147
	v_exp_f32_e32 v148, v148
	v_exp_f32_e32 v149, v149
	v_exp_f32_e32 v150, v150
	v_exp_f32_e32 v151, v151
	s_nop 0
	v_pk_add_f32 v[144:145], v[144:145], v[184:185]
	v_pk_add_f32 v[146:147], v[146:147], v[184:185]
	v_pk_add_f32 v[148:149], v[148:149], v[184:185]
	v_pk_add_f32 v[150:151], v[150:151], v[184:185]
	v_rcp_f32_e32 v144, v144
	v_rcp_f32_e32 v145, v145
	v_rcp_f32_e32 v146, v146
	v_rcp_f32_e32 v147, v147
	v_rcp_f32_e32 v148, v148
	v_rcp_f32_e32 v149, v149
	v_rcp_f32_e32 v150, v150
	v_rcp_f32_e32 v151, v151
	s_nop 0
	v_cvt_pk_bf16_f32 v46, v144, v145
	v_cvt_pk_bf16_f32 v47, v146, v147
	v_cvt_pk_bf16_f32 v48, v148, v149
	v_cvt_pk_bf16_f32 v49, v150, v151
	v_pk_mul_f32 v[38:39], v[38:39], v[140:141] op_sel:[0,1] op_sel_hi:[1,1]
	v_pk_mul_f32 v[40:41], v[40:41], v[140:141] op_sel:[0,1] op_sel_hi:[1,1]
	v_pk_mul_f32 v[34:35], v[34:35], v[140:141] op_sel:[0,1] op_sel_hi:[1,1]
	v_pk_mul_f32 v[36:37], v[36:37], v[140:141] op_sel:[0,1] op_sel_hi:[1,1]
	v_pk_mul_f32 v[144:145], v[38:39], v[186:187]
	v_pk_mul_f32 v[146:147], v[40:41], v[186:187]
	v_pk_mul_f32 v[148:149], v[34:35], v[186:187]
	v_pk_mul_f32 v[150:151], v[36:37], v[186:187]
	v_exp_f32_e32 v144, v144
	v_exp_f32_e32 v145, v145
	v_exp_f32_e32 v146, v146
	v_exp_f32_e32 v147, v147
	v_exp_f32_e32 v148, v148
	v_exp_f32_e32 v149, v149
	v_exp_f32_e32 v150, v150
	v_exp_f32_e32 v151, v151
	s_nop 0
	v_pk_add_f32 v[144:145], v[144:145], v[184:185]
	v_pk_add_f32 v[146:147], v[146:147], v[184:185]
	v_pk_add_f32 v[148:149], v[148:149], v[184:185]
	v_pk_add_f32 v[150:151], v[150:151], v[184:185]
	v_rcp_f32_e32 v144, v144
	v_rcp_f32_e32 v145, v145
	v_rcp_f32_e32 v146, v146
	v_rcp_f32_e32 v147, v147
	v_rcp_f32_e32 v148, v148
	v_rcp_f32_e32 v149, v149
	v_rcp_f32_e32 v150, v150
	v_rcp_f32_e32 v151, v151
	s_nop 0
	v_cvt_pk_bf16_f32 v38, v144, v145
	v_cvt_pk_bf16_f32 v39, v146, v147
	v_cvt_pk_bf16_f32 v40, v148, v149
	v_cvt_pk_bf16_f32 v41, v150, v151
	v_mov_b32_e32 v158, v38
	v_mov_b32_e32 v159, v39
	v_mov_b32_e32 v160, v40
	v_mov_b32_e32 v161, v41
	v_mov_b32_dpp v38, v46 row_shl:8 row_mask:0xf bank_mask:0x3
	v_mov_b32_dpp v39, v47 row_shl:8 row_mask:0xf bank_mask:0x3
	v_mov_b32_dpp v40, v48 row_shl:8 row_mask:0xf bank_mask:0x3
	v_mov_b32_dpp v41, v49 row_shl:8 row_mask:0xf bank_mask:0x3
	v_mov_b32_dpp v46, v158 row_shr:8 row_mask:0xf bank_mask:0xc
	v_mov_b32_dpp v47, v159 row_shr:8 row_mask:0xf bank_mask:0xc
	v_mov_b32_dpp v48, v160 row_shr:8 row_mask:0xf bank_mask:0xc
	v_mov_b32_dpp v49, v161 row_shr:8 row_mask:0xf bank_mask:0xc
	s_mul_i32 s28, s22, 144
	v_lshl_add_u64 v[180:181], s[28:29], 0, v[178:179]
	global_store_dwordx4 v[180:181], v[46:49], off nt
	s_mul_i32 s28, s22, 152
	v_lshl_add_u64 v[180:181], s[28:29], 0, v[178:179]
	global_store_dwordx4 v[180:181], v[38:41], off nt
	v_pk_mul_f32 v[30:31], v[30:31], v[142:143] op_sel_hi:[1,0]
	v_pk_mul_f32 v[32:33], v[32:33], v[142:143] op_sel_hi:[1,0]
	v_pk_mul_f32 v[26:27], v[26:27], v[142:143] op_sel_hi:[1,0]
	v_pk_mul_f32 v[28:29], v[28:29], v[142:143] op_sel_hi:[1,0]
	v_pk_mul_f32 v[144:145], v[30:31], v[186:187]
	v_pk_mul_f32 v[146:147], v[32:33], v[186:187]
	v_pk_mul_f32 v[148:149], v[26:27], v[186:187]
	v_pk_mul_f32 v[150:151], v[28:29], v[186:187]
	v_exp_f32_e32 v144, v144
	v_exp_f32_e32 v145, v145
	v_exp_f32_e32 v146, v146
	v_exp_f32_e32 v147, v147
	v_exp_f32_e32 v148, v148
	v_exp_f32_e32 v149, v149
	v_exp_f32_e32 v150, v150
	v_exp_f32_e32 v151, v151
	s_nop 0
	v_pk_add_f32 v[144:145], v[144:145], v[184:185]
	v_pk_add_f32 v[146:147], v[146:147], v[184:185]
	v_pk_add_f32 v[148:149], v[148:149], v[184:185]
	v_pk_add_f32 v[150:151], v[150:151], v[184:185]
	v_rcp_f32_e32 v144, v144
	v_rcp_f32_e32 v145, v145
	v_rcp_f32_e32 v146, v146
	v_rcp_f32_e32 v147, v147
	v_rcp_f32_e32 v148, v148
	v_rcp_f32_e32 v149, v149
	v_rcp_f32_e32 v150, v150
	v_rcp_f32_e32 v151, v151
	s_nop 0
	v_cvt_pk_bf16_f32 v30, v144, v145
	v_cvt_pk_bf16_f32 v31, v146, v147
	v_cvt_pk_bf16_f32 v32, v148, v149
	v_cvt_pk_bf16_f32 v33, v150, v151
	v_pk_mul_f32 v[22:23], v[22:23], v[142:143] op_sel_hi:[1,0]
	v_pk_mul_f32 v[24:25], v[24:25], v[142:143] op_sel_hi:[1,0]
	v_pk_mul_f32 v[18:19], v[18:19], v[142:143] op_sel_hi:[1,0]
	v_pk_mul_f32 v[20:21], v[20:21], v[142:143] op_sel_hi:[1,0]
	v_pk_mul_f32 v[144:145], v[22:23], v[186:187]
	v_pk_mul_f32 v[146:147], v[24:25], v[186:187]
	v_pk_mul_f32 v[148:149], v[18:19], v[186:187]
	v_pk_mul_f32 v[150:151], v[20:21], v[186:187]
	v_exp_f32_e32 v144, v144
	v_exp_f32_e32 v145, v145
	v_exp_f32_e32 v146, v146
	v_exp_f32_e32 v147, v147
	v_exp_f32_e32 v148, v148
	v_exp_f32_e32 v149, v149
	v_exp_f32_e32 v150, v150
	v_exp_f32_e32 v151, v151
	s_nop 0
	v_pk_add_f32 v[144:145], v[144:145], v[184:185]
	v_pk_add_f32 v[146:147], v[146:147], v[184:185]
	v_pk_add_f32 v[148:149], v[148:149], v[184:185]
	v_pk_add_f32 v[150:151], v[150:151], v[184:185]
	v_rcp_f32_e32 v144, v144
	v_rcp_f32_e32 v145, v145
	v_rcp_f32_e32 v146, v146
	v_rcp_f32_e32 v147, v147
	v_rcp_f32_e32 v148, v148
	v_rcp_f32_e32 v149, v149
	v_rcp_f32_e32 v150, v150
	v_rcp_f32_e32 v151, v151
	s_nop 0
	v_cvt_pk_bf16_f32 v22, v144, v145
	v_cvt_pk_bf16_f32 v23, v146, v147
	v_cvt_pk_bf16_f32 v24, v148, v149
	v_cvt_pk_bf16_f32 v25, v150, v151
	v_mov_b32_e32 v158, v22
	v_mov_b32_e32 v159, v23
	v_mov_b32_e32 v160, v24
	v_mov_b32_e32 v161, v25
	v_mov_b32_dpp v22, v30 row_shl:8 row_mask:0xf bank_mask:0x3
	v_mov_b32_dpp v23, v31 row_shl:8 row_mask:0xf bank_mask:0x3
	v_mov_b32_dpp v24, v32 row_shl:8 row_mask:0xf bank_mask:0x3
	v_mov_b32_dpp v25, v33 row_shl:8 row_mask:0xf bank_mask:0x3
	v_mov_b32_dpp v30, v158 row_shr:8 row_mask:0xf bank_mask:0xc
	v_mov_b32_dpp v31, v159 row_shr:8 row_mask:0xf bank_mask:0xc
	v_mov_b32_dpp v32, v160 row_shr:8 row_mask:0xf bank_mask:0xc
	v_mov_b32_dpp v33, v161 row_shr:8 row_mask:0xf bank_mask:0xc
	s_mul_i32 s28, s22, 160
	v_lshl_add_u64 v[180:181], s[28:29], 0, v[178:179]
	global_store_dwordx4 v[180:181], v[30:33], off nt
	s_mul_i32 s28, s22, 168
	v_lshl_add_u64 v[180:181], s[28:29], 0, v[178:179]
	global_store_dwordx4 v[180:181], v[22:25], off nt
	v_pk_mul_f32 v[14:15], v[14:15], v[142:143] op_sel:[0,1] op_sel_hi:[1,1]
	v_pk_mul_f32 v[16:17], v[16:17], v[142:143] op_sel:[0,1] op_sel_hi:[1,1]
	v_pk_mul_f32 v[10:11], v[10:11], v[142:143] op_sel:[0,1] op_sel_hi:[1,1]
	v_pk_mul_f32 v[12:13], v[12:13], v[142:143] op_sel:[0,1] op_sel_hi:[1,1]
	v_pk_mul_f32 v[144:145], v[14:15], v[186:187]
	v_pk_mul_f32 v[146:147], v[16:17], v[186:187]
	v_pk_mul_f32 v[148:149], v[10:11], v[186:187]
	v_pk_mul_f32 v[150:151], v[12:13], v[186:187]
	v_exp_f32_e32 v144, v144
	v_exp_f32_e32 v145, v145
	v_exp_f32_e32 v146, v146
	v_exp_f32_e32 v147, v147
	v_exp_f32_e32 v148, v148
	v_exp_f32_e32 v149, v149
	v_exp_f32_e32 v150, v150
	v_exp_f32_e32 v151, v151
	s_nop 0
	v_pk_add_f32 v[144:145], v[144:145], v[184:185]
	v_pk_add_f32 v[146:147], v[146:147], v[184:185]
	v_pk_add_f32 v[148:149], v[148:149], v[184:185]
	v_pk_add_f32 v[150:151], v[150:151], v[184:185]
	v_rcp_f32_e32 v144, v144
	v_rcp_f32_e32 v145, v145
	v_rcp_f32_e32 v146, v146
	v_rcp_f32_e32 v147, v147
	v_rcp_f32_e32 v148, v148
	v_rcp_f32_e32 v149, v149
	v_rcp_f32_e32 v150, v150
	v_rcp_f32_e32 v151, v151
	s_nop 0
	v_cvt_pk_bf16_f32 v14, v144, v145
	v_cvt_pk_bf16_f32 v15, v146, v147
	v_cvt_pk_bf16_f32 v16, v148, v149
	v_cvt_pk_bf16_f32 v17, v150, v151
	v_pk_mul_f32 v[6:7], v[6:7], v[142:143] op_sel:[0,1] op_sel_hi:[1,1]
	v_pk_mul_f32 v[8:9], v[8:9], v[142:143] op_sel:[0,1] op_sel_hi:[1,1]
	v_pk_mul_f32 v[2:3], v[2:3], v[142:143] op_sel:[0,1] op_sel_hi:[1,1]
	v_pk_mul_f32 v[4:5], v[4:5], v[142:143] op_sel:[0,1] op_sel_hi:[1,1]
	v_pk_mul_f32 v[144:145], v[6:7], v[186:187]
	v_pk_mul_f32 v[146:147], v[8:9], v[186:187]
	v_pk_mul_f32 v[148:149], v[2:3], v[186:187]
	v_pk_mul_f32 v[150:151], v[4:5], v[186:187]
	v_exp_f32_e32 v144, v144
	v_exp_f32_e32 v145, v145
	v_exp_f32_e32 v146, v146
	v_exp_f32_e32 v147, v147
	v_exp_f32_e32 v148, v148
	v_exp_f32_e32 v149, v149
	v_exp_f32_e32 v150, v150
	v_exp_f32_e32 v151, v151
	s_nop 0
	v_pk_add_f32 v[144:145], v[144:145], v[184:185]
	v_pk_add_f32 v[146:147], v[146:147], v[184:185]
	v_pk_add_f32 v[148:149], v[148:149], v[184:185]
	v_pk_add_f32 v[150:151], v[150:151], v[184:185]
	v_rcp_f32_e32 v144, v144
	v_rcp_f32_e32 v145, v145
	v_rcp_f32_e32 v146, v146
	v_rcp_f32_e32 v147, v147
	v_rcp_f32_e32 v148, v148
	v_rcp_f32_e32 v149, v149
	v_rcp_f32_e32 v150, v150
	v_rcp_f32_e32 v151, v151
	s_nop 0
	v_cvt_pk_bf16_f32 v6, v144, v145
	v_cvt_pk_bf16_f32 v7, v146, v147
	v_cvt_pk_bf16_f32 v8, v148, v149
	v_cvt_pk_bf16_f32 v9, v150, v151
	v_mov_b32_e32 v158, v6
	v_mov_b32_e32 v159, v7
	v_mov_b32_e32 v160, v8
	v_mov_b32_e32 v161, v9
	v_mov_b32_dpp v6, v14 row_shl:8 row_mask:0xf bank_mask:0x3
	v_mov_b32_dpp v7, v15 row_shl:8 row_mask:0xf bank_mask:0x3
	v_mov_b32_dpp v8, v16 row_shl:8 row_mask:0xf bank_mask:0x3
	v_mov_b32_dpp v9, v17 row_shl:8 row_mask:0xf bank_mask:0x3
	v_mov_b32_dpp v14, v158 row_shr:8 row_mask:0xf bank_mask:0xc
	v_mov_b32_dpp v15, v159 row_shr:8 row_mask:0xf bank_mask:0xc
	v_mov_b32_dpp v16, v160 row_shr:8 row_mask:0xf bank_mask:0xc
	v_mov_b32_dpp v17, v161 row_shr:8 row_mask:0xf bank_mask:0xc
	s_mul_i32 s28, s22, 176
	v_lshl_add_u64 v[180:181], s[28:29], 0, v[178:179]
	global_store_dwordx4 v[180:181], v[14:17], off nt
	s_mul_i32 s28, s22, 184
	v_lshl_add_u64 v[180:181], s[28:29], 0, v[178:179]
	global_store_dwordx4 v[180:181], v[6:9], off nt
